# speedup vs baseline: 1.0159x; 1.0013x over previous
_Z11k_conv_mfmaPKDF16_PKDv8_DF16_PKfS5_S5_S5_S5_PDF16_:
	s_load_dwordx4 s[8:11], s[0:1], 0x0
	s_load_dwordx8 s[36:43], s[0:1], 0x10
	s_bitcmp1_b32 s2, 3
	s_cbranch_scc0 .Lmy_conv_nosl
	s_sleep 6
.Lmy_conv_nosl:
	s_load_dwordx4 s[44:47], s[0:1], 0x30
	s_lshr_b32 s6, s2, 1
	v_readfirstlane_b32 s24, v0
	s_and_b32 s25, s2, 3
	s_and_b32 s3, s6, 2
	s_lshr_b32 s4, s2, 7
	s_lshr_b32 s2, s2, 3
	s_lshr_b32 s23, s24, 6
	s_add_i32 s7, s3, s4
	s_and_b32 s22, s2, 12
	s_mul_i32 s2, s25, 0x65400
	v_and_b32_e32 v1, 63, v0
	s_waitcnt lgkmcnt(0)
	s_lshl_b32 s21, s7, 2
	s_and_b32 s20, s6, 12
	s_add_i32 s12, s20, -1
	v_mul_u32_u24_e32 v16, 0xccd, v1
	v_add_u32_e32 v17, 64, v1
	v_lshrrev_b32_e32 v16, 16, v16
	v_mul_u32_u24_e32 v18, 0xccd, v17
	v_lshlrev_b32_e32 v19, 4, v1
	v_lshrrev_b32_e32 v18, 16, v18
	v_lshlrev_b32_e32 v21, 4, v17
	v_lshl_add_u32 v20, v16, 5, v19
	v_lshl_add_u32 v22, v18, 5, v21
	v_add_u32_e32 v23, s12, v16
	v_add_u32_e32 v17, s12, v18
	v_cmp_gt_u32_e64 s[14:15], 16, v23
	v_cmp_gt_u32_e64 s[16:17], 16, v17
	v_cmp_gt_u32_e64 s[18:19], 56, v1
	v_mov_b64_e32 v[24:25], 0
	v_mov_b64_e32 v[26:27], 0
	v_mov_b64_e32 v[28:29], 0
	v_mov_b64_e32 v[30:31], 0
	v_mov_b64_e32 v[32:33], 0
	v_mov_b64_e32 v[34:35], 0
	v_mov_b64_e32 v[36:37], 0
	v_mov_b64_e32 v[38:39], 0
	v_mov_b64_e32 v[40:41], 0
	v_mov_b64_e32 v[42:43], 0
	v_mov_b64_e32 v[44:45], 0
	v_mov_b64_e32 v[46:47], 0
	v_mov_b64_e32 v[102:103], 0
	v_mov_b64_e32 v[104:105], 0
	v_mov_b64_e32 v[106:107], 0
	v_mov_b64_e32 v[108:109], 0
	v_mov_b64_e32 v[110:111], 0
	v_mov_b64_e32 v[112:113], 0
	v_mov_b64_e32 v[114:115], 0
	v_mov_b64_e32 v[116:117], 0
	s_and_b64 s[16:17], s[16:17], s[18:19]
	s_add_i32 s26, s23, 0
	s_mul_i32 s27, s26, 43
	s_lshr_b32 s27, s27, 8
	s_mul_i32 s28, s27, 6
	s_sub_i32 s28, s26, s28
	s_add_i32 s27, s27, s21
	s_add_i32 s28, s28, s22
	s_add_i32 s27, s27, -1
	s_add_i32 s28, s28, -1
	s_or_b32 s29, s27, s28
	s_cmp_lt_u32 s29, 16
	s_cbranch_scc0 .Lmy_conv_skip0
	s_lshl_b32 s27, s27, 8
	s_lshl_b32 s28, s28, 4
	s_add_i32 s27, s27, s28
	s_add_i32 s27, s27, s12
	s_mulk_i32 s27, 0x140
	s_ashr_i32 s28, s27, 31
	s_add_u32 s34, s8, s27
	s_addc_u32 s35, s9, s28
	s_mov_b64 exec, s[14:15]
	global_load_dwordx4 v[24:27], v19, s[34:35]
	s_mov_b64 exec, s[16:17]
	global_load_dwordx4 v[28:31], v21, s[34:35]
	s_mov_b64 exec, -1
